# speedup vs baseline: 1.0155x; 1.0095x over previous
_Z11edge_kernelILi64ELb0EEvPKfS1_PKDF16_PKiS5_S1_S1_S1_S1_S1_PDF16_:
	s_load_dwordx16 s[4:19], s[0:1], 0x10
	s_load_dwordx2 s[20:21], s[0:1], 0x50
	v_readfirstlane_b32 s3, v0
	v_bfe_u32 v75, v0, 4, 2
	v_and_b32_e32 v76, 15, v0
	v_and_b32_e32 v78, 63, v0
	s_lshr_b32 s3, s3, 6
	s_lshl_b32 s2, s2, 1
	s_add_i32 s2, s2, s3
	v_lshlrev_b32_e32 v74, 8, v75
	v_lshl_or_b32 v74, v76, 4, v74
	v_lshlrev_b32_e32 v79, 4, v78
	v_lshl_or_b32 v77, v76, 2, v75
	v_lshlrev_b32_e32 v77, 2, v77
	v_lshlrev_b32_e32 v78, 5, v75
	v_lshlrev_b32_e32 v73, 12, v75
	v_lshl_or_b32 v73, v76, 4, v73
	s_lshl_b32 s28, s2, 14
	s_lshl_b32 s29, s2, 14
	s_lshl_b32 s30, s2, 2
	s_lshl_b32 s31, s2, 8
	s_lshl_b32 s33, s3, 10
	s_lshl_b32 s34, s3, 8
	s_addk_i32 s34, 0x4000
	s_waitcnt lgkmcnt(0)
	s_add_u32 s6, s6, s30
	s_addc_u32 s7, s7, 0
	s_add_u32 s8, s8, s30
	s_addc_u32 s9, s9, 0
	s_load_dword s35, s[6:7], 0x0
	s_load_dword s36, s[8:9], 0x0
	s_add_u32 s10, s10, s28
	s_addc_u32 s11, s11, 0
	s_add_u32 s18, s18, s33
	s_addc_u32 s19, s19, 0
	s_add_u32 s14, s14, s29
	s_addc_u32 s15, s15, 0
	s_add_u32 s12, s12, s31
	s_addc_u32 s13, s13, 0
	s_add_u32 s16, s16, s31
	s_addc_u32 s17, s17, 0
	s_waitcnt lgkmcnt(0)
	s_lshl_b32 s36, s36, 7
	s_add_u32 s20, s20, s36
	s_addc_u32 s21, s21, 0
	s_lshl_b32 s37, s35, 7
	s_add_u32 s4, s4, s37
	s_addc_u32 s5, s5, 0
	global_load_dwordx4 v[64:67], v78, s[4:5] nt
	global_load_dwordx4 v[68:71], v78, s[4:5] offset:16 nt
	v_add_u32_e32 v78, s34, v77
	s_waitcnt vmcnt(0)
	v_cvt_f32_f16_e32 v80, v64
	v_cvt_f32_f16_sdwa v81, v64 dst_sel:DWORD dst_unused:UNUSED_PAD src0_sel:WORD_1
	v_cvt_f32_f16_e32 v82, v65
	v_cvt_f32_f16_sdwa v83, v65 dst_sel:DWORD dst_unused:UNUSED_PAD src0_sel:WORD_1
	v_cvt_f32_f16_e32 v84, v66
	v_cvt_f32_f16_sdwa v85, v66 dst_sel:DWORD dst_unused:UNUSED_PAD src0_sel:WORD_1
	v_cvt_f32_f16_e32 v86, v67
	v_cvt_f32_f16_sdwa v87, v67 dst_sel:DWORD dst_unused:UNUSED_PAD src0_sel:WORD_1
	v_cvt_f32_f16_e32 v88, v68
	v_cvt_f32_f16_sdwa v89, v68 dst_sel:DWORD dst_unused:UNUSED_PAD src0_sel:WORD_1
	v_cvt_f32_f16_e32 v90, v69
	v_cvt_f32_f16_sdwa v91, v69 dst_sel:DWORD dst_unused:UNUSED_PAD src0_sel:WORD_1
	v_cvt_f32_f16_e32 v92, v70
	v_cvt_f32_f16_sdwa v93, v70 dst_sel:DWORD dst_unused:UNUSED_PAD src0_sel:WORD_1
	v_cvt_f32_f16_e32 v94, v71
	v_cvt_f32_f16_sdwa v95, v71 dst_sel:DWORD dst_unused:UNUSED_PAD src0_sel:WORD_1
	v_max_f32_e32 v80, 0, v80
	v_max_f32_e32 v81, 0, v81
	v_max_f32_e32 v82, 0, v82
	v_max_f32_e32 v83, 0, v83
	v_max_f32_e32 v84, 0, v84
	v_max_f32_e32 v85, 0, v85
	v_max_f32_e32 v86, 0, v86
	v_max_f32_e32 v87, 0, v87
	v_max_f32_e32 v88, 0, v88
	v_max_f32_e32 v89, 0, v89
	v_max_f32_e32 v90, 0, v90
	v_max_f32_e32 v91, 0, v91
	v_max_f32_e32 v92, 0, v92
	v_max_f32_e32 v93, 0, v93
	v_max_f32_e32 v94, 0, v94
	v_max_f32_e32 v95, 0, v95
	v_cmp_neq_f32_e64 s[40:41], 0, v80
	v_cmp_neq_f32_e64 s[42:43], 0, v81
	v_cmp_neq_f32_e64 s[44:45], 0, v82
	v_cmp_neq_f32_e64 s[46:47], 0, v83
	v_cmp_neq_f32_e64 s[48:49], 0, v84
	v_cmp_neq_f32_e64 s[50:51], 0, v85
	v_cmp_neq_f32_e64 s[52:53], 0, v86
	v_cmp_neq_f32_e64 s[54:55], 0, v87
	v_cmp_neq_f32_e64 s[56:57], 0, v88
	v_cmp_neq_f32_e64 s[58:59], 0, v89
	v_cmp_neq_f32_e64 s[60:61], 0, v90
	v_cmp_neq_f32_e64 s[62:63], 0, v91
	v_cmp_neq_f32_e64 s[64:65], 0, v92
	v_cmp_neq_f32_e64 s[66:67], 0, v93
	v_cmp_neq_f32_e64 s[68:69], 0, v94
	v_cmp_neq_f32_e64 s[70:71], 0, v95
	v_lshlrev_b32_e32 v96, 12, v75
	v_lshl_or_b32 v96, v76, 4, v96
	s_mov_b64 exec, s[40:41]
	global_load_dwordx4 v[0:3], v96, s[10:11] nt
	s_mov_b64 exec, s[42:43]
	global_load_dwordx4 v[4:7], v96, s[10:11] offset:256 nt
	s_mov_b64 exec, s[44:45]
	global_load_dwordx4 v[8:11], v96, s[10:11] offset:512 nt
	s_mov_b64 exec, s[46:47]
	global_load_dwordx4 v[12:15], v96, s[10:11] offset:768 nt
	s_mov_b64 exec, s[48:49]
	global_load_dwordx4 v[16:19], v96, s[10:11] offset:1024 nt
	s_mov_b64 exec, s[50:51]
	global_load_dwordx4 v[20:23], v96, s[10:11] offset:1280 nt
	s_mov_b64 exec, s[52:53]
	global_load_dwordx4 v[24:27], v96, s[10:11] offset:1536 nt
	s_mov_b64 exec, s[54:55]
	global_load_dwordx4 v[28:31], v96, s[10:11] offset:1792 nt
	s_mov_b64 exec, s[56:57]
	global_load_dwordx4 v[32:35], v96, s[10:11] offset:2048 nt
	s_mov_b64 exec, s[58:59]
	global_load_dwordx4 v[36:39], v96, s[10:11] offset:2304 nt
	s_mov_b64 exec, s[60:61]
	global_load_dwordx4 v[40:43], v96, s[10:11] offset:2560 nt
	s_mov_b64 exec, s[62:63]
	global_load_dwordx4 v[44:47], v96, s[10:11] offset:2816 nt
	s_mov_b64 exec, s[64:65]
	global_load_dwordx4 v[48:51], v96, s[10:11] offset:3072 nt
	s_mov_b64 exec, s[66:67]
	global_load_dwordx4 v[52:55], v96, s[10:11] offset:3328 nt
	s_mov_b64 exec, s[68:69]
	global_load_dwordx4 v[56:59], v96, s[10:11] offset:3584 nt
	s_mov_b64 exec, s[70:71]
	global_load_dwordx4 v[60:63], v96, s[10:11] offset:3840 nt
	s_mov_b64 exec, -1
	global_load_dword v72, v77, s[12:13] nt
	v_lshl_add_u32 v79, v75, 2, s34
	v_mov_b32_e32 v96, 0
	v_mov_b32_e32 v97, 0
	v_mov_b32_e32 v98, 0
	v_mov_b32_e32 v99, 0
	v_mov_b32_e32 v100, 0
	v_mov_b32_e32 v101, 0
	v_mov_b32_e32 v102, 0
	v_mov_b32_e32 v103, 0
	s_waitcnt vmcnt(0)
	s_mov_b64 exec, s[40:41]
	v_pk_fma_f32 v[96:97], v[80:81], v[0:1], v[96:97] op_sel_hi:[0,1,1]
	v_pk_fma_f32 v[98:99], v[80:81], v[2:3], v[98:99] op_sel_hi:[0,1,1]
	s_mov_b64 exec, s[42:43]
	v_pk_fma_f32 v[100:101], v[80:81], v[4:5], v[100:101] op_sel:[1,0,0]
	v_pk_fma_f32 v[102:103], v[80:81], v[6:7], v[102:103] op_sel:[1,0,0]
	s_mov_b64 exec, s[44:45]
	v_pk_fma_f32 v[96:97], v[82:83], v[8:9], v[96:97] op_sel_hi:[0,1,1]
	v_pk_fma_f32 v[98:99], v[82:83], v[10:11], v[98:99] op_sel_hi:[0,1,1]
	s_mov_b64 exec, s[46:47]
	v_pk_fma_f32 v[100:101], v[82:83], v[12:13], v[100:101] op_sel:[1,0,0]
	v_pk_fma_f32 v[102:103], v[82:83], v[14:15], v[102:103] op_sel:[1,0,0]
	s_mov_b64 exec, s[48:49]
	v_pk_fma_f32 v[96:97], v[84:85], v[16:17], v[96:97] op_sel_hi:[0,1,1]
	v_pk_fma_f32 v[98:99], v[84:85], v[18:19], v[98:99] op_sel_hi:[0,1,1]
	s_mov_b64 exec, s[50:51]
	v_pk_fma_f32 v[100:101], v[84:85], v[20:21], v[100:101] op_sel:[1,0,0]
	v_pk_fma_f32 v[102:103], v[84:85], v[22:23], v[102:103] op_sel:[1,0,0]
	s_mov_b64 exec, s[52:53]
	v_pk_fma_f32 v[96:97], v[86:87], v[24:25], v[96:97] op_sel_hi:[0,1,1]
	v_pk_fma_f32 v[98:99], v[86:87], v[26:27], v[98:99] op_sel_hi:[0,1,1]
	s_mov_b64 exec, s[54:55]
	v_pk_fma_f32 v[100:101], v[86:87], v[28:29], v[100:101] op_sel:[1,0,0]
	v_pk_fma_f32 v[102:103], v[86:87], v[30:31], v[102:103] op_sel:[1,0,0]
	s_mov_b64 exec, s[56:57]
	v_pk_fma_f32 v[96:97], v[88:89], v[32:33], v[96:97] op_sel_hi:[0,1,1]
	v_pk_fma_f32 v[98:99], v[88:89], v[34:35], v[98:99] op_sel_hi:[0,1,1]
	s_mov_b64 exec, s[58:59]
	v_pk_fma_f32 v[100:101], v[88:89], v[36:37], v[100:101] op_sel:[1,0,0]
	v_pk_fma_f32 v[102:103], v[88:89], v[38:39], v[102:103] op_sel:[1,0,0]
	s_mov_b64 exec, s[60:61]
	v_pk_fma_f32 v[96:97], v[90:91], v[40:41], v[96:97] op_sel_hi:[0,1,1]
	v_pk_fma_f32 v[98:99], v[90:91], v[42:43], v[98:99] op_sel_hi:[0,1,1]
	s_mov_b64 exec, s[62:63]
	v_pk_fma_f32 v[100:101], v[90:91], v[44:45], v[100:101] op_sel:[1,0,0]
	v_pk_fma_f32 v[102:103], v[90:91], v[46:47], v[102:103] op_sel:[1,0,0]
	s_mov_b64 exec, s[64:65]
	v_pk_fma_f32 v[96:97], v[92:93], v[48:49], v[96:97] op_sel_hi:[0,1,1]
	v_pk_fma_f32 v[98:99], v[92:93], v[50:51], v[98:99] op_sel_hi:[0,1,1]
	s_mov_b64 exec, s[66:67]
	v_pk_fma_f32 v[100:101], v[92:93], v[52:53], v[100:101] op_sel:[1,0,0]
	v_pk_fma_f32 v[102:103], v[92:93], v[54:55], v[102:103] op_sel:[1,0,0]
	s_mov_b64 exec, s[68:69]
	v_pk_fma_f32 v[96:97], v[94:95], v[56:57], v[96:97] op_sel_hi:[0,1,1]
	v_pk_fma_f32 v[98:99], v[94:95], v[58:59], v[98:99] op_sel_hi:[0,1,1]
	s_mov_b64 exec, s[70:71]
	v_pk_fma_f32 v[100:101], v[94:95], v[60:61], v[100:101] op_sel:[1,0,0]
	v_pk_fma_f32 v[102:103], v[94:95], v[62:63], v[102:103] op_sel:[1,0,0]
	s_mov_b64 exec, -1
	v_pk_add_f32 v[96:97], v[96:97], v[100:101]
	v_pk_add_f32 v[98:99], v[98:99], v[102:103]
	s_nop 1
	v_permlane16_swap_b32_e32 v96, v97
	v_permlane16_swap_b32_e32 v98, v99
	v_add_f32_e32 v96, v96, v97
	v_add_f32_e32 v98, v98, v99
	s_nop 1
	v_permlane32_swap_b32_e32 v96, v98
	v_add_f32_e32 v96, v96, v98
	s_waitcnt vmcnt(1)
	v_add_f32_e32 v96, v96, v72
	v_max_f32_e32 v96, 0, v96
	ds_write_b32 v78, v96
	ds_read2_b32 v[80:81], v79 offset0:0 offset1:4
	ds_read2_b32 v[82:83], v79 offset0:8 offset1:12
	ds_read2_b32 v[84:85], v79 offset0:16 offset1:20
	ds_read2_b32 v[86:87], v79 offset0:24 offset1:28
	ds_read2_b32 v[88:89], v79 offset0:32 offset1:36
	ds_read2_b32 v[90:91], v79 offset0:40 offset1:44
	ds_read2_b32 v[92:93], v79 offset0:48 offset1:52
	ds_read2_b32 v[94:95], v79 offset0:56 offset1:60
	s_waitcnt lgkmcnt(0)
	v_cmp_neq_f32_e64 s[40:41], 0, v80
	v_cmp_neq_f32_e64 s[42:43], 0, v81
	v_cmp_neq_f32_e64 s[44:45], 0, v82
	v_cmp_neq_f32_e64 s[46:47], 0, v83
	v_cmp_neq_f32_e64 s[48:49], 0, v84
	v_cmp_neq_f32_e64 s[50:51], 0, v85
	v_cmp_neq_f32_e64 s[52:53], 0, v86
	v_cmp_neq_f32_e64 s[54:55], 0, v87
	v_cmp_neq_f32_e64 s[56:57], 0, v88
	v_cmp_neq_f32_e64 s[58:59], 0, v89
	v_cmp_neq_f32_e64 s[60:61], 0, v90
	v_cmp_neq_f32_e64 s[62:63], 0, v91
	v_cmp_neq_f32_e64 s[64:65], 0, v92
	v_cmp_neq_f32_e64 s[66:67], 0, v93
	v_cmp_neq_f32_e64 s[68:69], 0, v94
	v_cmp_neq_f32_e64 s[70:71], 0, v95
	s_mov_b64 exec, s[40:41]
	global_load_dwordx4 v[0:3], v74, s[14:15] nt
	s_mov_b64 exec, s[42:43]
	global_load_dwordx4 v[4:7], v74, s[14:15] offset:1024 nt
	s_mov_b64 exec, s[44:45]
	global_load_dwordx4 v[8:11], v74, s[14:15] offset:2048 nt
	s_mov_b64 exec, s[46:47]
	global_load_dwordx4 v[12:15], v74, s[14:15] offset:3072 nt
	s_add_u32 s14, s14, 0x1000
	s_addc_u32 s15, s15, 0
	s_mov_b64 exec, s[48:49]
	global_load_dwordx4 v[16:19], v74, s[14:15] nt
	s_mov_b64 exec, s[50:51]
	global_load_dwordx4 v[20:23], v74, s[14:15] offset:1024 nt
	s_mov_b64 exec, s[52:53]
	global_load_dwordx4 v[24:27], v74, s[14:15] offset:2048 nt
	s_mov_b64 exec, s[54:55]
	global_load_dwordx4 v[28:31], v74, s[14:15] offset:3072 nt
	s_add_u32 s14, s14, 0x1000
	s_addc_u32 s15, s15, 0
	s_mov_b64 exec, s[56:57]
	global_load_dwordx4 v[32:35], v74, s[14:15] nt
	s_mov_b64 exec, s[58:59]
	global_load_dwordx4 v[36:39], v74, s[14:15] offset:1024 nt
	s_mov_b64 exec, s[60:61]
	global_load_dwordx4 v[40:43], v74, s[14:15] offset:2048 nt
	s_mov_b64 exec, s[62:63]
	global_load_dwordx4 v[44:47], v74, s[14:15] offset:3072 nt
	s_add_u32 s14, s14, 0x1000
	s_addc_u32 s15, s15, 0
	s_mov_b64 exec, s[64:65]
	global_load_dwordx4 v[48:51], v74, s[14:15] nt
	s_mov_b64 exec, s[66:67]
	global_load_dwordx4 v[52:55], v74, s[14:15] offset:1024 nt
	s_mov_b64 exec, s[68:69]
	global_load_dwordx4 v[56:59], v74, s[14:15] offset:2048 nt
	s_mov_b64 exec, s[70:71]
	global_load_dwordx4 v[60:63], v74, s[14:15] offset:3072 nt
	s_mov_b64 exec, -1
	global_load_dword v73, v77, s[16:17] nt
	s_mov_b32 m0, s33
	s_nop 0
	global_load_lds_dwordx4 v74, s[18:19]
	global_load_lds_dwordx4 v74, s[18:19] offset:2048
	s_add_u32 m0, m0, 0x1000
	s_add_u32 s18, s18, 0x1000
	s_addc_u32 s19, s19, 0
	global_load_lds_dwordx4 v74, s[18:19]
	global_load_lds_dwordx4 v74, s[18:19] offset:2048
	s_add_u32 m0, m0, 0x1000
	s_add_u32 s18, s18, 0x1000
	s_addc_u32 s19, s19, 0
	global_load_lds_dwordx4 v74, s[18:19]
	global_load_lds_dwordx4 v74, s[18:19] offset:2048
	s_add_u32 m0, m0, 0x1000
	s_add_u32 s18, s18, 0x1000
	s_addc_u32 s19, s19, 0
	global_load_lds_dwordx4 v74, s[18:19]
	global_load_lds_dwordx4 v74, s[18:19] offset:2048
	v_mov_b32_e32 v96, 0
	v_mov_b32_e32 v97, 0
	v_mov_b32_e32 v98, 0
	v_mov_b32_e32 v99, 0
	v_mov_b32_e32 v100, 0
	v_mov_b32_e32 v101, 0
	v_mov_b32_e32 v102, 0
	v_mov_b32_e32 v103, 0
	s_waitcnt vmcnt(9)
	s_mov_b64 exec, s[40:41]
	v_pk_fma_f32 v[96:97], v[80:81], v[0:1], v[96:97] op_sel_hi:[0,1,1]
	v_pk_fma_f32 v[98:99], v[80:81], v[2:3], v[98:99] op_sel_hi:[0,1,1]
	s_mov_b64 exec, s[42:43]
	v_pk_fma_f32 v[100:101], v[80:81], v[4:5], v[100:101] op_sel:[1,0,0]
	v_pk_fma_f32 v[102:103], v[80:81], v[6:7], v[102:103] op_sel:[1,0,0]
	s_mov_b64 exec, s[44:45]
	v_pk_fma_f32 v[96:97], v[82:83], v[8:9], v[96:97] op_sel_hi:[0,1,1]
	v_pk_fma_f32 v[98:99], v[82:83], v[10:11], v[98:99] op_sel_hi:[0,1,1]
	s_mov_b64 exec, s[46:47]
	v_pk_fma_f32 v[100:101], v[82:83], v[12:13], v[100:101] op_sel:[1,0,0]
	v_pk_fma_f32 v[102:103], v[82:83], v[14:15], v[102:103] op_sel:[1,0,0]
	s_mov_b64 exec, s[48:49]
	v_pk_fma_f32 v[96:97], v[84:85], v[16:17], v[96:97] op_sel_hi:[0,1,1]
	v_pk_fma_f32 v[98:99], v[84:85], v[18:19], v[98:99] op_sel_hi:[0,1,1]
	s_mov_b64 exec, s[50:51]
	v_pk_fma_f32 v[100:101], v[84:85], v[20:21], v[100:101] op_sel:[1,0,0]
	v_pk_fma_f32 v[102:103], v[84:85], v[22:23], v[102:103] op_sel:[1,0,0]
	s_mov_b64 exec, s[52:53]
	v_pk_fma_f32 v[96:97], v[86:87], v[24:25], v[96:97] op_sel_hi:[0,1,1]
	v_pk_fma_f32 v[98:99], v[86:87], v[26:27], v[98:99] op_sel_hi:[0,1,1]
	s_mov_b64 exec, s[54:55]
	v_pk_fma_f32 v[100:101], v[86:87], v[28:29], v[100:101] op_sel:[1,0,0]
	v_pk_fma_f32 v[102:103], v[86:87], v[30:31], v[102:103] op_sel:[1,0,0]
	s_mov_b64 exec, s[56:57]
	v_pk_fma_f32 v[96:97], v[88:89], v[32:33], v[96:97] op_sel_hi:[0,1,1]
	v_pk_fma_f32 v[98:99], v[88:89], v[34:35], v[98:99] op_sel_hi:[0,1,1]
	s_mov_b64 exec, s[58:59]
	v_pk_fma_f32 v[100:101], v[88:89], v[36:37], v[100:101] op_sel:[1,0,0]
	v_pk_fma_f32 v[102:103], v[88:89], v[38:39], v[102:103] op_sel:[1,0,0]
	s_mov_b64 exec, s[60:61]
	v_pk_fma_f32 v[96:97], v[90:91], v[40:41], v[96:97] op_sel_hi:[0,1,1]
	v_pk_fma_f32 v[98:99], v[90:91], v[42:43], v[98:99] op_sel_hi:[0,1,1]
	s_mov_b64 exec, s[62:63]
	v_pk_fma_f32 v[100:101], v[90:91], v[44:45], v[100:101] op_sel:[1,0,0]
	v_pk_fma_f32 v[102:103], v[90:91], v[46:47], v[102:103] op_sel:[1,0,0]
	s_mov_b64 exec, s[64:65]
	v_pk_fma_f32 v[96:97], v[92:93], v[48:49], v[96:97] op_sel_hi:[0,1,1]
	v_pk_fma_f32 v[98:99], v[92:93], v[50:51], v[98:99] op_sel_hi:[0,1,1]
	s_mov_b64 exec, s[66:67]
	v_pk_fma_f32 v[100:101], v[92:93], v[52:53], v[100:101] op_sel:[1,0,0]
	v_pk_fma_f32 v[102:103], v[92:93], v[54:55], v[102:103] op_sel:[1,0,0]
	s_mov_b64 exec, s[68:69]
	v_pk_fma_f32 v[96:97], v[94:95], v[56:57], v[96:97] op_sel_hi:[0,1,1]
	v_pk_fma_f32 v[98:99], v[94:95], v[58:59], v[98:99] op_sel_hi:[0,1,1]
	s_mov_b64 exec, s[70:71]
	v_pk_fma_f32 v[100:101], v[94:95], v[60:61], v[100:101] op_sel:[1,0,0]
	v_pk_fma_f32 v[102:103], v[94:95], v[62:63], v[102:103] op_sel:[1,0,0]
	s_mov_b64 exec, -1
	s_waitcnt vmcnt(0)
	s_barrier
	ds_read_b128 v[0:3], v74
	ds_read_b128 v[4:7], v74 offset:1024
	ds_read_b128 v[8:11], v74 offset:2048
	ds_read_b128 v[12:15], v74 offset:3072
	ds_read_b128 v[16:19], v74 offset:4096
	ds_read_b128 v[20:23], v74 offset:5120
	ds_read_b128 v[24:27], v74 offset:6144
	ds_read_b128 v[28:31], v74 offset:7168
	ds_read_b128 v[32:35], v74 offset:8192
	ds_read_b128 v[36:39], v74 offset:9216
	ds_read_b128 v[40:43], v74 offset:10240
	ds_read_b128 v[44:47], v74 offset:11264
	ds_read_b128 v[48:51], v74 offset:12288
	ds_read_b128 v[52:55], v74 offset:13312
	ds_read_b128 v[56:59], v74 offset:14336
	v_pk_add_f32 v[96:97], v[96:97], v[100:101]
	v_pk_add_f32 v[98:99], v[98:99], v[102:103]
	s_nop 1
	v_permlane16_swap_b32_e32 v96, v97
	v_permlane16_swap_b32_e32 v98, v99
	v_add_f32_e32 v96, v96, v97
	v_add_f32_e32 v98, v98, v99
	s_nop 1
	v_permlane32_swap_b32_e32 v96, v98
	v_add_f32_e32 v96, v96, v98
	v_add_f32_e32 v96, v96, v73
	s_waitcnt lgkmcnt(5)
	ds_read_b128 v[60:63], v74 offset:15360
	ds_write_b32 v78, v96
	ds_read2_b32 v[80:81], v79 offset0:0 offset1:4
	ds_read2_b32 v[82:83], v79 offset0:8 offset1:12
	ds_read2_b32 v[84:85], v79 offset0:16 offset1:20
	ds_read2_b32 v[86:87], v79 offset0:24 offset1:28
	ds_read2_b32 v[88:89], v79 offset0:32 offset1:36
	ds_read2_b32 v[90:91], v79 offset0:40 offset1:44
	ds_read2_b32 v[92:93], v79 offset0:48 offset1:52
	ds_read2_b32 v[94:95], v79 offset0:56 offset1:60
	v_lshlrev_b32_e32 v72, 3, v76
	v_lshl_or_b32 v72, v75, 2, v72
	v_cmp_gt_u32_e32 vcc, 2, v75
	s_waitcnt lgkmcnt(0)
	v_pk_mul_f32 v[96:97], v[80:81], v[0:1] op_sel_hi:[0,1]
	v_pk_mul_f32 v[98:99], v[80:81], v[2:3] op_sel_hi:[0,1]
	v_pk_mul_f32 v[100:101], v[80:81], v[4:5] op_sel:[1,0]
	v_pk_mul_f32 v[102:103], v[80:81], v[6:7] op_sel:[1,0]
	v_pk_fma_f32 v[96:97], v[82:83], v[8:9], v[96:97] op_sel_hi:[0,1,1]
	v_pk_fma_f32 v[98:99], v[82:83], v[10:11], v[98:99] op_sel_hi:[0,1,1]
	v_pk_fma_f32 v[100:101], v[82:83], v[12:13], v[100:101] op_sel:[1,0,0]
	v_pk_fma_f32 v[102:103], v[82:83], v[14:15], v[102:103] op_sel:[1,0,0]
	v_pk_fma_f32 v[96:97], v[84:85], v[16:17], v[96:97] op_sel_hi:[0,1,1]
	v_pk_fma_f32 v[98:99], v[84:85], v[18:19], v[98:99] op_sel_hi:[0,1,1]
	v_pk_fma_f32 v[100:101], v[84:85], v[20:21], v[100:101] op_sel:[1,0,0]
	v_pk_fma_f32 v[102:103], v[84:85], v[22:23], v[102:103] op_sel:[1,0,0]
	v_pk_fma_f32 v[96:97], v[86:87], v[24:25], v[96:97] op_sel_hi:[0,1,1]
	v_pk_fma_f32 v[98:99], v[86:87], v[26:27], v[98:99] op_sel_hi:[0,1,1]
	v_pk_fma_f32 v[100:101], v[86:87], v[28:29], v[100:101] op_sel:[1,0,0]
	v_pk_fma_f32 v[102:103], v[86:87], v[30:31], v[102:103] op_sel:[1,0,0]
	v_pk_fma_f32 v[96:97], v[88:89], v[32:33], v[96:97] op_sel_hi:[0,1,1]
	v_pk_fma_f32 v[98:99], v[88:89], v[34:35], v[98:99] op_sel_hi:[0,1,1]
	v_pk_fma_f32 v[100:101], v[88:89], v[36:37], v[100:101] op_sel:[1,0,0]
	v_pk_fma_f32 v[102:103], v[88:89], v[38:39], v[102:103] op_sel:[1,0,0]
	v_pk_fma_f32 v[96:97], v[90:91], v[40:41], v[96:97] op_sel_hi:[0,1,1]
	v_pk_fma_f32 v[98:99], v[90:91], v[42:43], v[98:99] op_sel_hi:[0,1,1]
	v_pk_fma_f32 v[100:101], v[90:91], v[44:45], v[100:101] op_sel:[1,0,0]
	v_pk_fma_f32 v[102:103], v[90:91], v[46:47], v[102:103] op_sel:[1,0,0]
	v_pk_fma_f32 v[96:97], v[92:93], v[48:49], v[96:97] op_sel_hi:[0,1,1]
	v_pk_fma_f32 v[98:99], v[92:93], v[50:51], v[98:99] op_sel_hi:[0,1,1]
	v_pk_fma_f32 v[100:101], v[92:93], v[52:53], v[100:101] op_sel:[1,0,0]
	v_pk_fma_f32 v[102:103], v[92:93], v[54:55], v[102:103] op_sel:[1,0,0]
	v_pk_fma_f32 v[96:97], v[94:95], v[56:57], v[96:97] op_sel_hi:[0,1,1]
	v_pk_fma_f32 v[98:99], v[94:95], v[58:59], v[98:99] op_sel_hi:[0,1,1]
	v_pk_fma_f32 v[100:101], v[94:95], v[60:61], v[100:101] op_sel:[1,0,0]
	v_pk_fma_f32 v[102:103], v[94:95], v[62:63], v[102:103] op_sel:[1,0,0]
	v_pk_add_f32 v[96:97], v[96:97], v[100:101]
	v_pk_add_f32 v[98:99], v[98:99], v[102:103]
	s_nop 1
	v_permlane16_swap_b32_e32 v96, v98
	v_permlane16_swap_b32_e32 v97, v99
	v_add_f32_e32 v96, v96, v98
	v_add_f32_e32 v97, v97, v99
	v_mov_b32_e32 v80, v96
	v_mov_b32_e32 v81, v97
	s_nop 1
	v_permlane32_swap_b32_e32 v96, v80
	v_permlane32_swap_b32_e32 v97, v81
	v_add_f32_e32 v96, v96, v80
	v_add_f32_e32 v97, v97, v81
	v_cvt_pk_f16_f32 v73, v96, v97
	s_and_saveexec_b64 s[4:5], vcc
	global_atomic_pk_add_f16 v72, v73, s[20:21]
	s_endpgm
	.p2align	8
